# speedup vs baseline: 1.0029x; 1.0009x over previous
.LBB5_21:
	s_add_i32 s1, s10, s0
	s_add_i32 s6, s1, -4
	s_min_u32 s1, s6, s1
	s_mul_i32 s6, s1, 0xc0
	v_add_u32_e32 v3, s6, v176
	ds_read_b128 v[178:181], v3
	ds_read_b128 v[182:185], v3 offset:64
	ds_read_b128 v[186:189], v3 offset:12544
	ds_read_b128 v[190:193], v3 offset:128
	ds_read_b128 v[194:197], v3 offset:12608
	ds_read_b128 v[198:201], v3 offset:12672
	s_mul_i32 s6, s1, 0x600
	s_addk_i32 s6, 0x600
	s_cmp_lt_i32 s1, 3
	s_cselect_b32 s6, s6, 0
	s_ashr_i32 s7, s6, 31
	s_setprio 1
	s_waitcnt vmcnt(17) lgkmcnt(5)
	v_mfma_f32_16x16x32_bf16 v[120:123], v[178:181], v[8:11], v[120:123]
	s_waitcnt lgkmcnt(3)
	v_mfma_f32_16x16x32_bf16 v[116:119], v[186:189], v[8:11], v[116:119]
	s_waitcnt vmcnt(16)
	v_mfma_f32_16x16x32_bf16 v[112:115], v[178:181], v[64:67], v[112:115]
	v_mfma_f32_16x16x32_bf16 v[108:111], v[186:189], v[64:67], v[108:111]
	s_waitcnt vmcnt(15)
	v_mfma_f32_16x16x32_bf16 v[104:107], v[178:181], v[68:71], v[104:107]
	v_mfma_f32_16x16x32_bf16 v[100:103], v[186:189], v[68:71], v[100:103]
	s_waitcnt vmcnt(14)
	v_mfma_f32_16x16x32_bf16 v[96:99], v[178:181], v[60:63], v[96:99]
	v_mfma_f32_16x16x32_bf16 v[92:95], v[186:189], v[60:63], v[92:95]
	s_waitcnt vmcnt(13)
	v_mfma_f32_16x16x32_bf16 v[88:91], v[178:181], v[72:75], v[88:91]
	v_mfma_f32_16x16x32_bf16 v[84:87], v[186:189], v[72:75], v[84:87]
	s_waitcnt vmcnt(12)
	v_mfma_f32_16x16x32_bf16 v[80:83], v[178:181], v[56:59], v[80:83]
	v_mfma_f32_16x16x32_bf16 v[76:79], v[186:189], v[56:59], v[76:79]
	s_setprio 0
	s_lshl_b64 s[6:7], s[6:7], 1
	v_lshl_add_u64 v[178:179], v[158:159], 0, s[6:7]
	v_lshl_add_u64 v[186:187], v[162:163], 0, s[6:7]
	v_lshl_add_u64 v[202:203], v[166:167], 0, s[6:7]
	v_lshl_add_u64 v[180:181], v[160:161], 0, s[6:7]
	global_load_dwordx4 v[8:11], v[178:179], off
	global_load_dwordx4 v[64:67], v[180:181], off
	v_lshl_add_u64 v[188:189], v[164:165], 0, s[6:7]
	global_load_dwordx4 v[68:71], v[186:187], off
	global_load_dwordx4 v[60:63], v[188:189], off
	v_lshl_add_u64 v[204:205], v[168:169], 0, s[6:7]
	global_load_dwordx4 v[72:75], v[202:203], off
	global_load_dwordx4 v[56:59], v[204:205], off
	s_setprio 1
	s_waitcnt vmcnt(17)
	v_mfma_f32_16x16x32_bf16 v[120:123], v[182:185], v[4:7], v[120:123]
	s_waitcnt lgkmcnt(1)
	v_mfma_f32_16x16x32_bf16 v[116:119], v[194:197], v[4:7], v[116:119]
	s_waitcnt vmcnt(16)
	v_mfma_f32_16x16x32_bf16 v[112:115], v[182:185], v[44:47], v[112:115]
	v_mfma_f32_16x16x32_bf16 v[108:111], v[194:197], v[44:47], v[108:111]
	s_waitcnt vmcnt(15)
	v_mfma_f32_16x16x32_bf16 v[104:107], v[182:185], v[52:55], v[104:107]
	v_mfma_f32_16x16x32_bf16 v[100:103], v[194:197], v[52:55], v[100:103]
	s_waitcnt vmcnt(14)
	v_mfma_f32_16x16x32_bf16 v[96:99], v[182:185], v[32:35], v[96:99]
	v_mfma_f32_16x16x32_bf16 v[92:95], v[194:197], v[32:35], v[92:95]
	s_waitcnt vmcnt(13)
	v_mfma_f32_16x16x32_bf16 v[88:91], v[182:185], v[48:51], v[88:91]
	v_mfma_f32_16x16x32_bf16 v[84:87], v[194:197], v[48:51], v[84:87]
	s_waitcnt vmcnt(12)
	v_mfma_f32_16x16x32_bf16 v[80:83], v[182:185], v[24:27], v[80:83]
	v_mfma_f32_16x16x32_bf16 v[76:79], v[194:197], v[24:27], v[76:79]
	s_setprio 0
	global_load_dwordx4 v[4:7], v[178:179], off offset:1024
	global_load_dwordx4 v[44:47], v[180:181], off offset:1024
	global_load_dwordx4 v[52:55], v[186:187], off offset:1024
	global_load_dwordx4 v[32:35], v[188:189], off offset:1024
	global_load_dwordx4 v[48:51], v[202:203], off offset:1024
	global_load_dwordx4 v[24:27], v[204:205], off offset:1024
	s_setprio 1
	s_waitcnt vmcnt(17)
	v_mfma_f32_16x16x32_bf16 v[120:123], v[190:193], v[40:43], v[120:123]
	s_waitcnt lgkmcnt(0)
	v_mfma_f32_16x16x32_bf16 v[116:119], v[198:201], v[40:43], v[116:119]
	s_waitcnt vmcnt(16)
	v_mfma_f32_16x16x32_bf16 v[112:115], v[190:193], v[28:31], v[112:115]
	v_mfma_f32_16x16x32_bf16 v[108:111], v[198:201], v[28:31], v[108:111]
	s_waitcnt vmcnt(15)
	v_mfma_f32_16x16x32_bf16 v[104:107], v[190:193], v[20:23], v[104:107]
	v_mfma_f32_16x16x32_bf16 v[100:103], v[198:201], v[20:23], v[100:103]
	s_waitcnt vmcnt(14)
	v_mfma_f32_16x16x32_bf16 v[96:99], v[190:193], v[16:19], v[96:99]
	v_mfma_f32_16x16x32_bf16 v[92:95], v[198:201], v[16:19], v[92:95]
	s_waitcnt vmcnt(13)
	v_mfma_f32_16x16x32_bf16 v[88:91], v[190:193], v[12:15], v[88:91]
	v_mfma_f32_16x16x32_bf16 v[84:87], v[198:201], v[12:15], v[84:87]
	s_waitcnt vmcnt(12)
	v_mfma_f32_16x16x32_bf16 v[80:83], v[190:193], v[36:39], v[80:83]
	v_mfma_f32_16x16x32_bf16 v[76:79], v[198:201], v[36:39], v[76:79]
	s_setprio 0
	global_load_dwordx4 v[40:43], v[178:179], off offset:2048
	global_load_dwordx4 v[28:31], v[180:181], off offset:2048
	global_load_dwordx4 v[20:23], v[186:187], off offset:2048
	global_load_dwordx4 v[16:19], v[188:189], off offset:2048
	global_load_dwordx4 v[12:15], v[202:203], off offset:2048
	global_load_dwordx4 v[36:39], v[204:205], off offset:2048
	s_add_i32 s0, s0, 1
	s_cmp_lg_u32 s0, 3
	s_cbranch_scc1 .LBB5_21
	s_mul_i32 s0, s10, 0x60
	s_add_i32 s6, s0, 0xffffffa0
	s_and_b64 s[0:1], s[2:3], exec
	s_cselect_b32 s0, 0x120, s6
	v_lshl_add_u32 v3, s0, 1, v175
	ds_read_b128 v[158:161], v3 offset:50176
	ds_read_b128 v[162:165], v3 offset:50240
	ds_read_b128 v[166:169], v3 offset:62720
	ds_read_b128 v[178:181], v3 offset:50304
	ds_read_b128 v[182:185], v3 offset:62784
	ds_read_b128 v[186:189], v3 offset:62848
	s_setprio 1
	s_waitcnt vmcnt(17) lgkmcnt(5)
	v_mfma_f32_16x16x32_bf16 v[120:123], v[158:161], v[8:11], v[120:123]
	s_waitcnt lgkmcnt(3)
	v_mfma_f32_16x16x32_bf16 v[8:11], v[166:169], v[8:11], v[116:119]
	s_waitcnt vmcnt(16)
	v_mfma_f32_16x16x32_bf16 v[112:115], v[158:161], v[64:67], v[112:115]
	v_mfma_f32_16x16x32_bf16 v[64:67], v[166:169], v[64:67], v[108:111]
	s_waitcnt vmcnt(15)
	v_mfma_f32_16x16x32_bf16 v[104:107], v[158:161], v[68:71], v[104:107]
	v_mfma_f32_16x16x32_bf16 v[68:71], v[166:169], v[68:71], v[100:103]
	s_waitcnt vmcnt(14)
	v_mfma_f32_16x16x32_bf16 v[96:99], v[158:161], v[60:63], v[96:99]
	v_mfma_f32_16x16x32_bf16 v[60:63], v[166:169], v[60:63], v[92:95]
	s_waitcnt vmcnt(13)
	v_mfma_f32_16x16x32_bf16 v[88:91], v[158:161], v[72:75], v[88:91]
	v_mfma_f32_16x16x32_bf16 v[72:75], v[166:169], v[72:75], v[84:87]
	s_waitcnt vmcnt(12)
	v_mfma_f32_16x16x32_bf16 v[80:83], v[158:161], v[56:59], v[80:83]
	v_mfma_f32_16x16x32_bf16 v[56:59], v[166:169], v[56:59], v[76:79]
	s_setprio 0
	s_setprio 1
	s_waitcnt vmcnt(11)
	v_mfma_f32_16x16x32_bf16 v[76:79], v[162:165], v[4:7], v[120:123]
	s_waitcnt lgkmcnt(1)
	v_mfma_f32_16x16x32_bf16 v[4:7], v[182:185], v[4:7], v[8:11]
	s_waitcnt vmcnt(10)
	v_mfma_f32_16x16x32_bf16 v[8:11], v[162:165], v[44:47], v[112:115]
	v_mfma_f32_16x16x32_bf16 v[44:47], v[182:185], v[44:47], v[64:67]
	s_waitcnt vmcnt(9)
	v_mfma_f32_16x16x32_bf16 v[64:67], v[162:165], v[52:55], v[104:107]
	v_mfma_f32_16x16x32_bf16 v[52:55], v[182:185], v[52:55], v[68:71]
	s_waitcnt vmcnt(8)
	v_mfma_f32_16x16x32_bf16 v[68:71], v[162:165], v[32:35], v[96:99]
	v_mfma_f32_16x16x32_bf16 v[60:63], v[182:185], v[32:35], v[60:63]
	s_waitcnt vmcnt(7)
	v_mfma_f32_16x16x32_bf16 v[84:87], v[162:165], v[48:51], v[88:91]
	v_mfma_f32_16x16x32_bf16 v[48:51], v[182:185], v[48:51], v[72:75]
	s_waitcnt vmcnt(6)
	v_mfma_f32_16x16x32_bf16 v[72:75], v[162:165], v[24:27], v[80:83]
	v_mfma_f32_16x16x32_bf16 v[56:59], v[182:185], v[24:27], v[56:59]
	s_setprio 0
	s_setprio 1
	s_waitcnt vmcnt(5) lgkmcnt(0)
	v_mfma_f32_16x16x32_bf16 v[116:119], v[186:189], v[40:43], v[4:7]
	s_waitcnt vmcnt(4)
	v_mfma_f32_16x16x32_bf16 v[112:115], v[178:181], v[28:31], v[8:11]
	v_mfma_f32_16x16x32_bf16 v[108:111], v[186:189], v[28:31], v[44:47]
	s_waitcnt vmcnt(3)
	v_mfma_f32_16x16x32_bf16 v[32:35], v[178:181], v[20:23], v[64:67]
	v_mfma_f32_16x16x32_bf16 v[28:31], v[186:189], v[20:23], v[52:55]
	s_waitcnt vmcnt(2)
	v_mfma_f32_16x16x32_bf16 v[24:27], v[178:181], v[16:19], v[68:71]
	v_mfma_f32_16x16x32_bf16 v[20:23], v[186:189], v[16:19], v[60:63]
	s_waitcnt vmcnt(1)
	v_mfma_f32_16x16x32_bf16 v[16:19], v[178:181], v[12:15], v[84:87]
	v_mfma_f32_16x16x32_bf16 v[12:15], v[186:189], v[12:15], v[48:51]
	s_waitcnt vmcnt(0)
	v_mfma_f32_16x16x32_bf16 v[8:11], v[178:181], v[36:39], v[72:75]
	v_mfma_f32_16x16x32_bf16 v[4:7], v[186:189], v[36:39], v[56:59]
	v_mfma_f32_16x16x32_bf16 v[120:123], v[178:181], v[40:43], v[76:79]
	s_setprio 0
	v_or_b32_e32 v37, v177, v171
	v_lshlrev_b32_e32 v36, 2, v37
	global_load_dword v158, v36, s[24:25]
	s_lshl_b32 s0, s11, 1
	s_add_u32 s0, s22, s0
	s_addc_u32 s1, s23, 0
	v_add_u32_e32 v163, v177, v171
	s_add_u32 s8, s0, 0x1000
	v_lshlrev_b64 v[154:155], 1, v[154:155]
	v_lshlrev_b64 v[156:157], 1, v[156:157]
	v_lshlrev_b32_e32 v166, 1, v37
	v_lshlrev_b32_e32 v37, 2, v163
	s_addc_u32 s9, s1, 0
	global_load_dword v164, v36, s[24:25] offset:64
	global_load_dword v159, v37, s[24:25] offset:128
	global_load_dword v161, v37, s[24:25] offset:192
	global_load_dword v162, v37, s[24:25] offset:256
	global_load_dword v160, v37, s[24:25] offset:320
	v_lshl_add_u64 v[40:41], s[0:1], 0, v[154:155]
	v_lshl_add_u64 v[42:43], s[0:1], 0, v[156:157]
	global_load_dwordx4 v[92:95], v2, s[0:1]
	global_load_dwordx4 v[72:75], v2, s[0:1] offset:1024
	global_load_dwordx4 v[52:55], v2, s[0:1] offset:2048
	global_load_dwordx4 v[36:39], v2, s[0:1] offset:3072
	s_add_u32 s0, s0, 0x1400
	global_load_dwordx4 v[104:107], v[40:41], off
	global_load_dwordx4 v[84:87], v[40:41], off offset:1024
	global_load_dwordx4 v[100:103], v[42:43], off
	global_load_dwordx4 v[76:79], v[42:43], off offset:1024
	global_load_dwordx4 v[60:63], v[40:41], off offset:2048
	global_load_dwordx4 v[48:51], v[40:41], off offset:3072
	global_load_dwordx4 v[56:59], v[42:43], off offset:2048
	global_load_dwordx4 v[44:47], v[42:43], off offset:3072
	v_lshl_add_u64 v[40:41], s[8:9], 0, v[154:155]
	v_lshl_add_u64 v[42:43], s[8:9], 0, v[156:157]
	s_addc_u32 s1, s1, 0
	global_load_dwordx4 v[64:67], v[40:41], off
	global_load_dwordx4 v[68:71], v[42:43], off
	global_load_dwordx4 v[80:83], v2, s[8:9]
	s_nop 0
	global_load_dwordx4 v[40:43], v2, s[0:1]
	v_lshl_add_u64 v[88:89], s[0:1], 0, v[154:155]
	v_lshl_add_u64 v[90:91], s[0:1], 0, v[156:157]
	s_movk_i32 s7, 0x1840
	v_mad_u32_u24 v165, v170, s7, v166
	v_mov_b32_e32 v3, 0
	s_mov_b32 s6, 0
	s_waitcnt vmcnt(21)
	v_add_f32_e32 v120, v158, v120
	v_add_f32_e32 v121, v158, v121
	v_mul_f32_e32 v96, 0x3d372713, v120
	v_mul_f32_e32 v97, 0x3d372713, v121
	v_mul_f32_e32 v96, v120, v96
	v_mul_f32_e32 v97, v121, v97
	v_fma_f32 v96, v120, v96, v120
	v_fma_f32 v97, v121, v97, v121
	v_mul_f32_e32 v96, 0x3f4c422a, v96
	v_mul_f32_e32 v97, 0x3f4c422a, v97
	v_mul_f32_e32 v96, 0xc038aa3b, v96
	v_mul_f32_e32 v97, 0xc038aa3b, v97
	v_exp_f32_e32 v167, v96
	v_exp_f32_e32 v168, v97
	v_add_f32_e32 v122, v158, v122
	v_mul_f32_e32 v98, 0x3d372713, v122
	v_add_f32_e32 v167, 1.0, v167
	v_add_f32_e32 v168, 1.0, v168
	v_div_scale_f32 v175, s[0:1], v167, v167, v120
	v_mul_f32_e32 v98, v122, v98
	v_div_scale_f32 v177, s[0:1], v168, v168, v121
	v_rcp_f32_e32 v179, v175
	v_fma_f32 v98, v122, v98, v122
	v_rcp_f32_e32 v180, v177
	v_mul_f32_e32 v98, 0x3f4c422a, v98
	v_mul_f32_e32 v98, 0xc038aa3b, v98
	v_fma_f32 v183, -v175, v179, 1.0
	v_exp_f32_e32 v169, v98
	v_div_scale_f32 v176, vcc, v120, v167, v120
	v_fma_f32 v184, -v177, v180, 1.0
	v_fmac_f32_e32 v179, v183, v179
	v_div_scale_f32 v178, s[0:1], v121, v168, v121
	v_fmac_f32_e32 v180, v184, v180
	v_mul_f32_e32 v183, v176, v179
	v_mul_f32_e32 v184, v178, v180
	v_fma_f32 v185, -v175, v183, v176
	v_fma_f32 v186, -v177, v184, v178
	v_fmac_f32_e32 v183, v185, v179
	v_add_f32_e32 v169, 1.0, v169
	v_fmac_f32_e32 v184, v186, v180
	v_fma_f32 v175, -v175, v183, v176
	v_div_scale_f32 v181, s[8:9], v169, v169, v122
	v_fma_f32 v176, -v177, v184, v178
	v_div_fmas_f32 v175, v175, v179, v183
	s_mov_b64 vcc, s[0:1]
	v_rcp_f32_e32 v182, v181
	v_div_fixup_f32 v120, v175, v167, v120
	v_div_fmas_f32 v167, v176, v180, v184
	v_cvt_pk_bf16_f32 v120, v120, s0
	v_div_fixup_f32 v121, v167, v168, v121
	global_load_dwordx4 v[96:99], v[88:89], off
	s_nop 0
	global_load_dwordx4 v[88:91], v[90:91], off
	ds_write_b16 v165, v120
	v_cvt_pk_bf16_f32 v120, v121, s0
	s_movk_i32 s0, 0x610
	v_mad_u32_u24 v121, v174, s0, v166
	ds_write_b16 v121, v120
	v_fma_f32 v120, -v181, v182, 1.0
	v_fmac_f32_e32 v182, v120, v182
	v_div_scale_f32 v120, vcc, v122, v169, v122
	v_mul_f32_e32 v167, v120, v182
	v_fma_f32 v168, -v181, v167, v120
	v_add_f32_e32 v123, v158, v123
	v_fmac_f32_e32 v167, v168, v182
	v_mul_f32_e32 v168, 0x3d372713, v123
	v_mul_f32_e32 v168, v123, v168
	v_fma_f32 v168, v123, v168, v123
	v_mul_f32_e32 v168, 0x3f4c422a, v168
	v_mul_f32_e32 v168, 0xc038aa3b, v168
	v_exp_f32_e32 v168, v168
	v_fma_f32 v120, -v181, v167, v120
	v_div_fmas_f32 v120, v120, v182, v167
	v_div_fixup_f32 v120, v120, v169, v122
	v_add_f32_e32 v122, 1.0, v168
	v_div_scale_f32 v167, s[8:9], v122, v122, v123
	v_rcp_f32_e32 v168, v167
	v_mad_u32_u24 v169, v174, s0, s0
	v_cvt_pk_bf16_f32 v120, v120, s0
	v_add_u32_e32 v175, v166, v169
	ds_write_b16 v175, v120
	v_fma_f32 v120, -v167, v168, 1.0
	v_fmac_f32_e32 v168, v120, v168
	v_div_scale_f32 v120, vcc, v123, v122, v123
	v_mul_f32_e32 v176, v120, v168
	v_fma_f32 v177, -v167, v176, v120
	v_fmac_f32_e32 v176, v177, v168
	v_add_f32_e32 v116, v158, v116
	v_fma_f32 v120, -v167, v176, v120
	v_mul_f32_e32 v167, 0x3d372713, v116
	v_mul_f32_e32 v167, v116, v167
	v_fma_f32 v167, v116, v167, v116
	v_mul_f32_e32 v167, 0x3f4c422a, v167
	v_mul_f32_e32 v167, 0xc038aa3b, v167
	v_exp_f32_e32 v167, v167
	v_div_fmas_f32 v120, v120, v168, v176
	v_div_fixup_f32 v120, v120, v122, v123
	v_mov_b32_e32 v122, 0xc20
	v_add_f32_e32 v123, 1.0, v167
	v_div_scale_f32 v167, s[8:9], v123, v123, v116
	v_rcp_f32_e32 v168, v167
	v_mad_u32_u24 v122, v174, s0, v122
	v_cvt_pk_bf16_f32 v120, v120, s0
	v_add_u32_e32 v176, v166, v122
	ds_write_b16 v176, v120
	v_fma_f32 v120, -v167, v168, 1.0
	v_fmac_f32_e32 v168, v120, v168
	v_div_scale_f32 v120, vcc, v116, v123, v116
	v_mul_f32_e32 v177, v120, v168
	v_fma_f32 v178, -v167, v177, v120
	v_fmac_f32_e32 v177, v178, v168
	v_add_f32_e32 v117, v158, v117
	v_fma_f32 v120, -v167, v177, v120
	v_mul_f32_e32 v167, 0x3d372713, v117
	v_mul_f32_e32 v167, v117, v167
	v_fma_f32 v167, v117, v167, v117
	v_mul_f32_e32 v167, 0x3f4c422a, v167
	v_mul_f32_e32 v167, 0xc038aa3b, v167
	v_exp_f32_e32 v167, v167
	v_div_fmas_f32 v120, v120, v168, v177
	v_div_fixup_f32 v116, v120, v123, v116
	v_mov_b32_e32 v120, 0x5af0
	v_add_f32_e32 v123, 1.0, v167
	v_div_scale_f32 v167, s[8:9], v123, v123, v117
	v_rcp_f32_e32 v168, v167
	v_mad_u32_u24 v120, v174, s0, v120
	v_cvt_pk_bf16_f32 v116, v116, s0
	v_add_u32_e32 v177, v166, v120
	ds_write_b16 v177, v116
	v_fma_f32 v116, -v167, v168, 1.0
	v_fmac_f32_e32 v168, v116, v168
	v_div_scale_f32 v116, vcc, v117, v123, v117
	v_mul_f32_e32 v178, v116, v168
	v_fma_f32 v179, -v167, v178, v116
	v_fmac_f32_e32 v178, v179, v168
	v_add_f32_e32 v118, v158, v118
	v_fma_f32 v116, -v167, v178, v116
	v_mul_f32_e32 v167, 0x3d372713, v118
	v_mul_f32_e32 v167, v118, v167
	v_fma_f32 v167, v118, v167, v118
	v_mul_f32_e32 v167, 0x3f4c422a, v167
	v_mul_f32_e32 v167, 0xc038aa3b, v167
	v_exp_f32_e32 v167, v167
	v_div_fmas_f32 v116, v116, v168, v178
	v_div_fixup_f32 v116, v116, v123, v117
	v_add_f32_e32 v119, v158, v119
	v_add_f32_e32 v123, 1.0, v167
	v_div_scale_f32 v167, s[8:9], v123, v123, v118
	v_rcp_f32_e32 v168, v167
	v_mov_b32_e32 v117, 0x6100
	v_mul_f32_e32 v158, 0x3d372713, v119
	v_mad_u32_u24 v117, v174, s0, v117
	v_mul_f32_e32 v158, v119, v158
	v_cvt_pk_bf16_f32 v116, v116, s0
	v_add_u32_e32 v178, v166, v117
	v_fma_f32 v158, v119, v158, v119
	ds_write_b16 v178, v116
	v_fma_f32 v116, -v167, v168, 1.0
	v_mul_f32_e32 v158, 0x3f4c422a, v158
	v_fmac_f32_e32 v168, v116, v168
	v_div_scale_f32 v116, vcc, v118, v123, v118
	v_mul_f32_e32 v179, v116, v168
	v_mul_f32_e32 v158, 0xc038aa3b, v158
	v_fma_f32 v180, -v167, v179, v116
	v_exp_f32_e32 v158, v158
	v_fmac_f32_e32 v179, v180, v168
	v_fma_f32 v116, -v167, v179, v116
	v_div_fmas_f32 v116, v116, v168, v179
	v_div_fixup_f32 v116, v116, v123, v118
	v_add_f32_e32 v123, 1.0, v158
	v_div_scale_f32 v158, s[8:9], v123, v123, v119
	v_rcp_f32_e32 v167, v158
	v_mov_b32_e32 v118, 0x6710
	v_mad_u32_u24 v118, v174, s0, v118
	v_cvt_pk_bf16_f32 v116, v116, s0
	v_add_u32_e32 v168, v166, v118
	ds_write_b16 v168, v116
	v_fma_f32 v116, -v158, v167, 1.0
	v_fmac_f32_e32 v167, v116, v167
	v_div_scale_f32 v116, vcc, v119, v123, v119
	v_mul_f32_e32 v179, v116, v167
	v_fma_f32 v180, -v158, v179, v116
	v_fmac_f32_e32 v179, v180, v167
	s_waitcnt vmcnt(22)
	v_add_f32_e32 v112, v164, v112
	v_fma_f32 v116, -v158, v179, v116
	v_mul_f32_e32 v158, 0x3d372713, v112
	v_mul_f32_e32 v158, v112, v158
	v_fma_f32 v158, v112, v158, v112
	v_mul_f32_e32 v158, 0x3f4c422a, v158
	v_mul_f32_e32 v158, 0xc038aa3b, v158
	v_exp_f32_e32 v158, v158
	v_div_fmas_f32 v116, v116, v167, v179
	v_div_fixup_f32 v116, v116, v123, v119
	v_mov_b32_e32 v119, 0x6d20
	v_add_f32_e32 v123, 1.0, v158
	v_div_scale_f32 v158, s[8:9], v123, v123, v112
	v_rcp_f32_e32 v167, v158
	v_mad_u32_u24 v119, v174, s0, v119
	v_cvt_pk_bf16_f32 v116, v116, s0
	v_add_u32_e32 v166, v166, v119
	ds_write_b16 v166, v116
	v_fma_f32 v116, -v158, v167, 1.0
	v_fmac_f32_e32 v167, v116, v167
	v_div_scale_f32 v116, vcc, v112, v123, v112
	v_mul_f32_e32 v179, v116, v167
	v_fma_f32 v180, -v158, v179, v116
	v_add_f32_e32 v113, v164, v113
	v_fmac_f32_e32 v179, v180, v167
	v_mul_f32_e32 v180, 0x3d372713, v113
	v_mul_f32_e32 v180, v113, v180
	v_fma_f32 v180, v113, v180, v113
	v_mul_f32_e32 v180, 0x3f4c422a, v180
	v_mul_f32_e32 v180, 0xc038aa3b, v180
	v_exp_f32_e32 v180, v180
	v_fma_f32 v116, -v158, v179, v116
	v_div_fmas_f32 v116, v116, v167, v179
	v_div_fixup_f32 v112, v116, v123, v112
	v_add_f32_e32 v158, 1.0, v180
	v_div_scale_f32 v167, s[8:9], v158, v158, v113
	v_rcp_f32_e32 v179, v167
	v_cvt_pk_bf16_f32 v112, v112, s0
	ds_write_b16 v165, v112 offset:32
	v_add_f32_e32 v114, v164, v114
	v_fma_f32 v112, -v167, v179, 1.0
	v_fmac_f32_e32 v179, v112, v179
	v_div_scale_f32 v112, vcc, v113, v158, v113
	v_mul_f32_e32 v116, v112, v179
	v_fma_f32 v123, -v167, v116, v112
	v_fmac_f32_e32 v116, v123, v179
	v_mul_f32_e32 v123, 0x3d372713, v114
	v_mul_f32_e32 v123, v114, v123
	v_fma_f32 v123, v114, v123, v114
	v_mul_f32_e32 v123, 0x3f4c422a, v123
	v_mul_f32_e32 v123, 0xc038aa3b, v123
	v_exp_f32_e32 v123, v123
	v_fma_f32 v112, -v167, v116, v112
	v_div_fmas_f32 v112, v112, v179, v116
	v_div_fixup_f32 v112, v112, v158, v113
	v_add_f32_e32 v116, 1.0, v123
	v_div_scale_f32 v123, s[8:9], v116, v116, v114
	v_rcp_f32_e32 v165, v123
	v_cvt_pk_bf16_f32 v112, v112, s0
	ds_write_b16 v121, v112 offset:32
	v_add_f32_e32 v115, v164, v115
	v_fma_f32 v112, -v123, v165, 1.0
	v_fmac_f32_e32 v165, v112, v165
	v_div_scale_f32 v112, vcc, v114, v116, v114
	v_mul_f32_e32 v113, v112, v165
	v_fma_f32 v121, -v123, v113, v112
	v_fmac_f32_e32 v113, v121, v165
	v_mul_f32_e32 v121, 0x3d372713, v115
	v_mul_f32_e32 v121, v115, v121
	v_fma_f32 v121, v115, v121, v115
	v_mul_f32_e32 v121, 0x3f4c422a, v121
	v_mul_f32_e32 v121, 0xc038aa3b, v121
	v_exp_f32_e32 v121, v121
	v_fma_f32 v112, -v123, v113, v112
	v_div_fmas_f32 v112, v112, v165, v113
	v_div_fixup_f32 v112, v112, v116, v114
	v_add_f32_e32 v113, 1.0, v121
	v_div_scale_f32 v121, s[8:9], v113, v113, v115
	v_rcp_f32_e32 v123, v121
	v_cvt_pk_bf16_f32 v112, v112, s0
	ds_write_b16 v175, v112 offset:32
	v_add_f32_e32 v108, v164, v108
	v_fma_f32 v112, -v121, v123, 1.0
	v_fmac_f32_e32 v123, v112, v123
	v_div_scale_f32 v112, vcc, v115, v113, v115
	v_mul_f32_e32 v114, v112, v123
	v_fma_f32 v116, -v121, v114, v112
	v_fmac_f32_e32 v114, v116, v123
	v_mul_f32_e32 v116, 0x3d372713, v108
	v_mul_f32_e32 v116, v108, v116
	v_fma_f32 v116, v108, v116, v108
	v_mul_f32_e32 v116, 0x3f4c422a, v116
	v_mul_f32_e32 v116, 0xc038aa3b, v116
	v_exp_f32_e32 v116, v116
	v_fma_f32 v112, -v121, v114, v112
	v_div_fmas_f32 v112, v112, v123, v114
	v_div_fixup_f32 v112, v112, v113, v115
	v_add_f32_e32 v114, 1.0, v116
	v_div_scale_f32 v116, s[8:9], v114, v114, v108
	v_rcp_f32_e32 v121, v116
	v_cvt_pk_bf16_f32 v112, v112, s0
	ds_write_b16 v176, v112 offset:32
	v_add_f32_e32 v109, v164, v109
	v_fma_f32 v112, -v116, v121, 1.0
	v_fmac_f32_e32 v121, v112, v121
	v_div_scale_f32 v112, vcc, v108, v114, v108
	v_mul_f32_e32 v113, v112, v121
	v_fma_f32 v115, -v116, v113, v112
	v_fmac_f32_e32 v113, v115, v121
	v_mul_f32_e32 v115, 0x3d372713, v109
	v_mul_f32_e32 v115, v109, v115
	v_fma_f32 v115, v109, v115, v109
	v_mul_f32_e32 v115, 0x3f4c422a, v115
	v_mul_f32_e32 v115, 0xc038aa3b, v115
	v_exp_f32_e32 v115, v115
	v_fma_f32 v112, -v116, v113, v112
	v_div_fmas_f32 v112, v112, v121, v113
	v_div_fixup_f32 v108, v112, v114, v108
	v_add_f32_e32 v113, 1.0, v115
	v_div_scale_f32 v115, s[8:9], v113, v113, v109
	v_rcp_f32_e32 v116, v115
	v_cvt_pk_bf16_f32 v108, v108, s0
	ds_write_b16 v177, v108 offset:32
	v_add_f32_e32 v110, v164, v110
	v_fma_f32 v108, -v115, v116, 1.0
	v_fmac_f32_e32 v116, v108, v116
	v_div_scale_f32 v108, vcc, v109, v113, v109
	v_mul_f32_e32 v112, v108, v116
	v_fma_f32 v114, -v115, v112, v108
	v_fmac_f32_e32 v112, v114, v116
	v_mul_f32_e32 v114, 0x3d372713, v110
	v_mul_f32_e32 v114, v110, v114
	v_fma_f32 v114, v110, v114, v110
	v_mul_f32_e32 v114, 0x3f4c422a, v114
	v_mul_f32_e32 v114, 0xc038aa3b, v114
	v_exp_f32_e32 v114, v114
	v_fma_f32 v108, -v115, v112, v108
	v_div_fmas_f32 v108, v108, v116, v112
	v_div_fixup_f32 v108, v108, v113, v109
	v_add_f32_e32 v112, 1.0, v114
	v_div_scale_f32 v114, s[8:9], v112, v112, v110
	v_rcp_f32_e32 v115, v114
	v_cvt_pk_bf16_f32 v108, v108, s0
	ds_write_b16 v178, v108 offset:32
	v_add_f32_e32 v111, v164, v111
	v_fma_f32 v108, -v114, v115, 1.0
	v_fmac_f32_e32 v115, v108, v115
	v_div_scale_f32 v108, vcc, v110, v112, v110
	v_mul_f32_e32 v109, v108, v115
	v_fma_f32 v113, -v114, v109, v108
	v_fmac_f32_e32 v109, v113, v115
	v_mul_f32_e32 v113, 0x3d372713, v111
	v_mul_f32_e32 v113, v111, v113
	v_fma_f32 v113, v111, v113, v111
	v_mul_f32_e32 v113, 0x3f4c422a, v113
	v_mul_f32_e32 v113, 0xc038aa3b, v113
	v_exp_f32_e32 v113, v113
	v_fma_f32 v108, -v114, v109, v108
	v_div_fmas_f32 v108, v108, v115, v109
	v_div_fixup_f32 v108, v108, v112, v110
	v_add_f32_e32 v109, 1.0, v113
	v_div_scale_f32 v113, s[8:9], v109, v109, v111
	v_rcp_f32_e32 v114, v113
	v_cvt_pk_bf16_f32 v108, v108, s0
	ds_write_b16 v168, v108 offset:32
	s_waitcnt vmcnt(21)
	v_add_f32_e32 v32, v159, v32
	v_fma_f32 v108, -v113, v114, 1.0
	v_fmac_f32_e32 v114, v108, v114
	v_div_scale_f32 v108, vcc, v111, v109, v111
	v_mul_f32_e32 v110, v108, v114
	v_fma_f32 v112, -v113, v110, v108
	v_fmac_f32_e32 v110, v112, v114
	v_mul_f32_e32 v112, 0x3d372713, v32
	v_mul_f32_e32 v112, v32, v112
	v_fma_f32 v112, v32, v112, v32
	v_mul_f32_e32 v112, 0x3f4c422a, v112
	v_mul_f32_e32 v112, 0xc038aa3b, v112
	v_exp_f32_e32 v112, v112
	v_fma_f32 v108, -v113, v110, v108
	v_div_fmas_f32 v108, v108, v114, v110
	v_div_fixup_f32 v108, v108, v109, v111
	v_add_f32_e32 v109, 1.0, v112
	v_div_scale_f32 v110, s[8:9], v109, v109, v32
	v_rcp_f32_e32 v111, v110
	v_cvt_pk_bf16_f32 v108, v108, s0
	ds_write_b16 v166, v108 offset:32
	v_add_f32_e32 v33, v159, v33
	v_fma_f32 v108, -v110, v111, 1.0
	v_fmac_f32_e32 v111, v108, v111
	v_div_scale_f32 v108, vcc, v32, v109, v32
	v_mul_f32_e32 v113, v108, v111
	v_fma_f32 v114, -v110, v113, v108
	v_fmac_f32_e32 v113, v114, v111
	v_fma_f32 v108, -v110, v113, v108
	v_mul_f32_e32 v110, 0x3d372713, v33
	v_mul_f32_e32 v110, v33, v110
	v_fma_f32 v110, v33, v110, v33
	v_mul_f32_e32 v110, 0x3f4c422a, v110
	v_mul_f32_e32 v110, 0xc038aa3b, v110
	v_exp_f32_e32 v110, v110
	v_div_fmas_f32 v108, v108, v111, v113
	v_div_fixup_f32 v32, v108, v109, v32
	v_lshlrev_b32_e32 v112, 1, v163
	v_add_f32_e32 v108, 1.0, v110
	v_div_scale_f32 v110, s[8:9], v108, v108, v33
	v_rcp_f32_e32 v111, v110
	v_cvt_pk_bf16_f32 v32, v32, s0
	v_mad_u32_u24 v109, v170, s7, v112
	ds_write_b16 v109, v32 offset:64
	v_fma_f32 v32, -v110, v111, 1.0
	v_fmac_f32_e32 v111, v32, v111
	v_div_scale_f32 v32, vcc, v33, v108, v33
	v_mul_f32_e32 v113, v32, v111
	v_fma_f32 v114, -v110, v113, v32
	v_fmac_f32_e32 v113, v114, v111
	v_add_f32_e32 v34, v159, v34
	v_fma_f32 v32, -v110, v113, v32
	v_mul_f32_e32 v110, 0x3d372713, v34
	v_mul_f32_e32 v110, v34, v110
	v_fma_f32 v110, v34, v110, v34
	v_mul_f32_e32 v110, 0x3f4c422a, v110
	v_mul_f32_e32 v110, 0xc038aa3b, v110
	v_exp_f32_e32 v110, v110
	v_div_fmas_f32 v32, v32, v111, v113
	v_div_fixup_f32 v32, v32, v108, v33
	v_cvt_pk_bf16_f32 v32, v32, s0
	v_add_f32_e32 v33, 1.0, v110
	v_div_scale_f32 v110, s[8:9], v33, v33, v34
	v_rcp_f32_e32 v111, v110
	v_mad_u32_u24 v108, v174, s0, v112
	ds_write_b16 v108, v32 offset:64
	v_add_f32_e32 v35, v159, v35
	v_fma_f32 v32, -v110, v111, 1.0
	v_fmac_f32_e32 v111, v32, v111
	v_div_scale_f32 v32, vcc, v34, v33, v34
	v_mul_f32_e32 v113, v32, v111
	v_fma_f32 v114, -v110, v113, v32
	v_fmac_f32_e32 v113, v114, v111
	v_fma_f32 v32, -v110, v113, v32
	v_mul_f32_e32 v110, 0x3d372713, v35
	v_mul_f32_e32 v110, v35, v110
	v_fma_f32 v110, v35, v110, v35
	v_mul_f32_e32 v110, 0x3f4c422a, v110
	v_mul_f32_e32 v110, 0xc038aa3b, v110
	v_exp_f32_e32 v110, v110
	v_div_fmas_f32 v32, v32, v111, v113
	v_div_fixup_f32 v32, v32, v33, v34
	v_add_u32_e32 v34, v112, v169
	v_add_f32_e32 v33, 1.0, v110
	v_div_scale_f32 v110, s[0:1], v33, v33, v35
	v_rcp_f32_e32 v111, v110
	s_nop 0
	v_cvt_pk_bf16_f32 v32, v32, s0
	ds_write_b16 v34, v32 offset:64
	v_add_f32_e32 v28, v159, v28
	v_fma_f32 v32, -v110, v111, 1.0
	v_fmac_f32_e32 v111, v32, v111
	v_div_scale_f32 v32, vcc, v35, v33, v35
	v_mul_f32_e32 v113, v32, v111
	v_fma_f32 v114, -v110, v113, v32
	v_fmac_f32_e32 v113, v114, v111
	v_fma_f32 v32, -v110, v113, v32
	v_mul_f32_e32 v110, 0x3d372713, v28
	v_mul_f32_e32 v110, v28, v110
	v_fma_f32 v110, v28, v110, v28
	v_mul_f32_e32 v110, 0x3f4c422a, v110
	v_mul_f32_e32 v110, 0xc038aa3b, v110
	v_exp_f32_e32 v110, v110
	v_div_fmas_f32 v32, v32, v111, v113
	v_div_fixup_f32 v32, v32, v33, v35
	v_add_u32_e32 v33, v112, v122
	v_add_f32_e32 v35, 1.0, v110
	v_div_scale_f32 v110, s[0:1], v35, v35, v28
	v_rcp_f32_e32 v111, v110
	s_nop 0
	v_cvt_pk_bf16_f32 v32, v32, s0
	ds_write_b16 v33, v32 offset:64
	v_add_f32_e32 v29, v159, v29
	v_fma_f32 v32, -v110, v111, 1.0
	v_fmac_f32_e32 v111, v32, v111
	v_div_scale_f32 v32, vcc, v28, v35, v28
	v_mul_f32_e32 v113, v32, v111
	v_fma_f32 v114, -v110, v113, v32
	v_fmac_f32_e32 v113, v114, v111
	v_fma_f32 v32, -v110, v113, v32
	v_mul_f32_e32 v110, 0x3d372713, v29
	v_mul_f32_e32 v110, v29, v110
	v_fma_f32 v110, v29, v110, v29
	v_mul_f32_e32 v110, 0x3f4c422a, v110
	v_mul_f32_e32 v110, 0xc038aa3b, v110
	v_exp_f32_e32 v110, v110
	v_div_fmas_f32 v32, v32, v111, v113
	v_div_fixup_f32 v28, v32, v35, v28
	v_add_u32_e32 v32, v112, v120
	v_add_f32_e32 v35, 1.0, v110
	v_div_scale_f32 v110, s[0:1], v35, v35, v29
	v_rcp_f32_e32 v111, v110
	s_nop 0
	v_cvt_pk_bf16_f32 v28, v28, s0
	ds_write_b16 v32, v28 offset:64
	v_add_f32_e32 v30, v159, v30
	v_fma_f32 v28, -v110, v111, 1.0
	v_fmac_f32_e32 v111, v28, v111
	v_div_scale_f32 v28, vcc, v29, v35, v29
	v_mul_f32_e32 v113, v28, v111
	v_fma_f32 v114, -v110, v113, v28
	v_fmac_f32_e32 v113, v114, v111
	v_fma_f32 v28, -v110, v113, v28
	v_mul_f32_e32 v110, 0x3d372713, v30
	v_mul_f32_e32 v110, v30, v110
	v_fma_f32 v110, v30, v110, v30
	v_mul_f32_e32 v110, 0x3f4c422a, v110
	v_mul_f32_e32 v110, 0xc038aa3b, v110
	v_exp_f32_e32 v110, v110
	v_div_fmas_f32 v28, v28, v111, v113
	v_div_fixup_f32 v28, v28, v35, v29
	v_add_u32_e32 v29, v112, v117
	v_add_f32_e32 v35, 1.0, v110
	v_div_scale_f32 v110, s[0:1], v35, v35, v30
	v_rcp_f32_e32 v111, v110
	s_nop 0
	v_cvt_pk_bf16_f32 v28, v28, s0
	ds_write_b16 v29, v28 offset:64
	v_add_f32_e32 v31, v159, v31
	v_fma_f32 v28, -v110, v111, 1.0
	v_fmac_f32_e32 v111, v28, v111
	v_div_scale_f32 v28, vcc, v30, v35, v30
	v_mul_f32_e32 v113, v28, v111
	v_fma_f32 v114, -v110, v113, v28
	v_fmac_f32_e32 v113, v114, v111
	v_fma_f32 v28, -v110, v113, v28
	v_mul_f32_e32 v110, 0x3d372713, v31
	v_mul_f32_e32 v110, v31, v110
	v_fma_f32 v110, v31, v110, v31
	v_mul_f32_e32 v110, 0x3f4c422a, v110
	v_mul_f32_e32 v110, 0xc038aa3b, v110
	v_exp_f32_e32 v110, v110
	v_div_fmas_f32 v28, v28, v111, v113
	v_div_fixup_f32 v28, v28, v35, v30
	s_waitcnt vmcnt(20)
	v_add_f32_e32 v25, v161, v25
	v_add_f32_e32 v30, 1.0, v110
	v_div_scale_f32 v35, s[0:1], v30, v30, v31
	v_rcp_f32_e32 v110, v35
	s_nop 0
	v_cvt_pk_bf16_f32 v111, v28, s0
	v_add_u32_e32 v28, v112, v118
	ds_write_b16 v28, v111 offset:64
	v_fma_f32 v111, -v35, v110, 1.0
	v_fmac_f32_e32 v110, v111, v110
	v_div_scale_f32 v111, vcc, v31, v30, v31
	v_mul_f32_e32 v113, v111, v110
	v_fma_f32 v114, -v35, v113, v111
	v_fmac_f32_e32 v113, v114, v110
	v_fma_f32 v35, -v35, v113, v111
	v_add_f32_e32 v111, v161, v24
	v_mul_f32_e32 v24, 0x3d372713, v111
	v_mul_f32_e32 v24, v111, v24
	v_fma_f32 v24, v111, v24, v111
	v_mul_f32_e32 v24, 0x3f4c422a, v24
	v_mul_f32_e32 v24, 0xc038aa3b, v24
	v_exp_f32_e32 v24, v24
	v_div_fmas_f32 v35, v35, v110, v113
	v_div_fixup_f32 v30, v35, v30, v31
	v_add_f32_e32 v26, v161, v26
	v_add_f32_e32 v31, 1.0, v24
	v_div_scale_f32 v35, s[0:1], v31, v31, v111
	v_rcp_f32_e32 v110, v35
	s_nop 0
	v_cvt_pk_bf16_f32 v30, v30, s0
	v_add_u32_e32 v24, v112, v119
	ds_write_b16 v24, v30 offset:64
	v_fma_f32 v30, -v35, v110, 1.0
	v_fmac_f32_e32 v110, v30, v110
	v_div_scale_f32 v30, vcc, v111, v31, v111
	v_mul_f32_e32 v112, v30, v110
	v_fma_f32 v113, -v35, v112, v30
	v_fmac_f32_e32 v112, v113, v110
	v_mul_f32_e32 v113, 0x3d372713, v25
	v_mul_f32_e32 v113, v25, v113
	v_fma_f32 v113, v25, v113, v25
	v_mul_f32_e32 v113, 0x3f4c422a, v113
	v_mul_f32_e32 v113, 0xc038aa3b, v113
	v_exp_f32_e32 v113, v113
	v_fma_f32 v30, -v35, v112, v30
	v_div_fmas_f32 v30, v30, v110, v112
	v_div_fixup_f32 v30, v30, v31, v111
	v_add_f32_e32 v35, 1.0, v113
	v_div_scale_f32 v110, s[0:1], v35, v35, v25
	v_rcp_f32_e32 v112, v110
	s_nop 0
	v_cvt_pk_bf16_f32 v30, v30, s0
	ds_write_b16 v109, v30 offset:96
	v_add_f32_e32 v27, v161, v27
	v_fma_f32 v30, -v110, v112, 1.0
	v_fmac_f32_e32 v112, v30, v112
	v_div_scale_f32 v30, vcc, v25, v35, v25
	v_mul_f32_e32 v31, v30, v112
	v_fma_f32 v111, -v110, v31, v30
	v_fmac_f32_e32 v31, v111, v112
	v_mul_f32_e32 v111, 0x3d372713, v26
	v_mul_f32_e32 v111, v26, v111
	v_fma_f32 v111, v26, v111, v26
	v_mul_f32_e32 v111, 0x3f4c422a, v111
	v_mul_f32_e32 v111, 0xc038aa3b, v111
	v_exp_f32_e32 v111, v111
	v_fma_f32 v30, -v110, v31, v30
	v_div_fmas_f32 v30, v30, v112, v31
	v_div_fixup_f32 v25, v30, v35, v25
	v_add_f32_e32 v31, 1.0, v111
	v_div_scale_f32 v110, s[0:1], v31, v31, v26
	v_rcp_f32_e32 v111, v110
	s_nop 0
	v_cvt_pk_bf16_f32 v25, v25, s0
	ds_write_b16 v108, v25 offset:96
	v_add_f32_e32 v20, v161, v20
	v_fma_f32 v25, -v110, v111, 1.0
	v_fmac_f32_e32 v111, v25, v111
	v_div_scale_f32 v25, vcc, v26, v31, v26
	v_mul_f32_e32 v30, v25, v111
	v_fma_f32 v35, -v110, v30, v25
	v_fmac_f32_e32 v30, v35, v111
	v_mul_f32_e32 v35, 0x3d372713, v27
	v_mul_f32_e32 v35, v27, v35
	v_fma_f32 v35, v27, v35, v27
	v_mul_f32_e32 v35, 0x3f4c422a, v35
	v_mul_f32_e32 v35, 0xc038aa3b, v35
	v_exp_f32_e32 v35, v35
	v_fma_f32 v25, -v110, v30, v25
	v_div_fmas_f32 v25, v25, v111, v30
	v_div_fixup_f32 v25, v25, v31, v26
	v_add_f32_e32 v30, 1.0, v35
	v_div_scale_f32 v35, s[0:1], v30, v30, v27
	v_rcp_f32_e32 v110, v35
	s_nop 0
	v_cvt_pk_bf16_f32 v25, v25, s0
	ds_write_b16 v34, v25 offset:96
	v_add_f32_e32 v21, v161, v21
	v_fma_f32 v25, -v35, v110, 1.0
	v_fmac_f32_e32 v110, v25, v110
	v_div_scale_f32 v25, vcc, v27, v30, v27
	v_mul_f32_e32 v26, v25, v110
	v_fma_f32 v31, -v35, v26, v25
	v_fmac_f32_e32 v26, v31, v110
	v_mul_f32_e32 v31, 0x3d372713, v20
	v_mul_f32_e32 v31, v20, v31
	v_fma_f32 v31, v20, v31, v20
	v_mul_f32_e32 v31, 0x3f4c422a, v31
	v_mul_f32_e32 v31, 0xc038aa3b, v31
	v_exp_f32_e32 v31, v31
	v_fma_f32 v25, -v35, v26, v25
	v_div_fmas_f32 v25, v25, v110, v26
	v_div_fixup_f32 v25, v25, v30, v27
	v_add_f32_e32 v26, 1.0, v31
	v_div_scale_f32 v31, s[0:1], v26, v26, v20
	v_rcp_f32_e32 v35, v31
	s_nop 0
	v_cvt_pk_bf16_f32 v25, v25, s0
	ds_write_b16 v33, v25 offset:96
	v_add_f32_e32 v22, v161, v22
	v_fma_f32 v25, -v31, v35, 1.0
	v_fmac_f32_e32 v35, v25, v35
	v_div_scale_f32 v25, vcc, v20, v26, v20
	v_mul_f32_e32 v27, v25, v35
	v_fma_f32 v30, -v31, v27, v25
	v_fmac_f32_e32 v27, v30, v35
	v_mul_f32_e32 v30, 0x3d372713, v21
	v_mul_f32_e32 v30, v21, v30
	v_fma_f32 v30, v21, v30, v21
	v_mul_f32_e32 v30, 0x3f4c422a, v30
	v_mul_f32_e32 v30, 0xc038aa3b, v30
	v_exp_f32_e32 v30, v30
	v_fma_f32 v25, -v31, v27, v25
	v_div_fmas_f32 v25, v25, v35, v27
	v_div_fixup_f32 v20, v25, v26, v20
	v_add_f32_e32 v27, 1.0, v30
	v_div_scale_f32 v30, s[0:1], v27, v27, v21
	v_rcp_f32_e32 v31, v30
	s_nop 0
	v_cvt_pk_bf16_f32 v20, v20, s0
	ds_write_b16 v32, v20 offset:96
	v_add_f32_e32 v23, v161, v23
	v_fma_f32 v20, -v30, v31, 1.0
	v_fmac_f32_e32 v31, v20, v31
	v_div_scale_f32 v20, vcc, v21, v27, v21
	v_mul_f32_e32 v25, v20, v31
	v_fma_f32 v26, -v30, v25, v20
	v_fmac_f32_e32 v25, v26, v31
	v_mul_f32_e32 v26, 0x3d372713, v22
	v_mul_f32_e32 v26, v22, v26
	v_fma_f32 v26, v22, v26, v22
	v_mul_f32_e32 v26, 0x3f4c422a, v26
	v_mul_f32_e32 v26, 0xc038aa3b, v26
	v_exp_f32_e32 v26, v26
	v_fma_f32 v20, -v30, v25, v20
	v_div_fmas_f32 v20, v20, v31, v25
	v_div_fixup_f32 v20, v20, v27, v21
	v_add_f32_e32 v25, 1.0, v26
	v_div_scale_f32 v26, s[0:1], v25, v25, v22
	v_rcp_f32_e32 v30, v26
	s_nop 0
	v_cvt_pk_bf16_f32 v20, v20, s0
	ds_write_b16 v29, v20 offset:96
	s_waitcnt vmcnt(19)
	v_add_f32_e32 v16, v162, v16
	v_fma_f32 v20, -v26, v30, 1.0
	v_fmac_f32_e32 v30, v20, v30
	v_div_scale_f32 v20, vcc, v22, v25, v22
	v_mul_f32_e32 v21, v20, v30
	v_fma_f32 v27, -v26, v21, v20
	v_fmac_f32_e32 v21, v27, v30
	v_mul_f32_e32 v27, 0x3d372713, v23
	v_mul_f32_e32 v27, v23, v27
	v_fma_f32 v27, v23, v27, v23
	v_mul_f32_e32 v27, 0x3f4c422a, v27
	v_mul_f32_e32 v27, 0xc038aa3b, v27
	v_exp_f32_e32 v27, v27
	v_fma_f32 v20, -v26, v21, v20
	v_div_fmas_f32 v20, v20, v30, v21
	v_div_fixup_f32 v20, v20, v25, v22
	v_add_f32_e32 v21, 1.0, v27
	v_div_scale_f32 v26, s[0:1], v21, v21, v23
	v_rcp_f32_e32 v27, v26
	s_nop 0
	v_cvt_pk_bf16_f32 v20, v20, s0
	ds_write_b16 v28, v20 offset:96
	v_add_f32_e32 v17, v162, v17
	v_fma_f32 v20, -v26, v27, 1.0
	v_fmac_f32_e32 v27, v20, v27
	v_div_scale_f32 v20, vcc, v23, v21, v23
	v_mul_f32_e32 v22, v20, v27
	v_fma_f32 v25, -v26, v22, v20
	v_fmac_f32_e32 v22, v25, v27
	v_mul_f32_e32 v25, 0x3d372713, v16
	v_mul_f32_e32 v25, v16, v25
	v_fma_f32 v25, v16, v25, v16
	v_mul_f32_e32 v25, 0x3f4c422a, v25
	v_mul_f32_e32 v25, 0xc038aa3b, v25
	v_exp_f32_e32 v25, v25
	v_fma_f32 v20, -v26, v22, v20
	v_div_fmas_f32 v20, v20, v27, v22
	v_div_fixup_f32 v20, v20, v21, v23
	v_add_f32_e32 v22, 1.0, v25
	v_div_scale_f32 v25, s[0:1], v22, v22, v16
	v_rcp_f32_e32 v26, v25
	s_nop 0
	v_cvt_pk_bf16_f32 v20, v20, s0
	ds_write_b16 v24, v20 offset:96
	v_add_f32_e32 v18, v162, v18
	v_fma_f32 v20, -v25, v26, 1.0
	v_fmac_f32_e32 v26, v20, v26
	v_div_scale_f32 v20, vcc, v16, v22, v16
	v_mul_f32_e32 v21, v20, v26
	v_fma_f32 v23, -v25, v21, v20
	v_fmac_f32_e32 v21, v23, v26
	v_mul_f32_e32 v23, 0x3d372713, v17
	v_mul_f32_e32 v23, v17, v23
	v_fma_f32 v23, v17, v23, v17
	v_mul_f32_e32 v23, 0x3f4c422a, v23
	v_mul_f32_e32 v23, 0xc038aa3b, v23
	v_exp_f32_e32 v23, v23
	v_fma_f32 v20, -v25, v21, v20
	v_div_fmas_f32 v20, v20, v26, v21
	v_div_fixup_f32 v16, v20, v22, v16
	v_add_f32_e32 v21, 1.0, v23
	v_div_scale_f32 v23, s[0:1], v21, v21, v17
	v_rcp_f32_e32 v25, v23
	s_nop 0
	v_cvt_pk_bf16_f32 v16, v16, s0
	ds_write_b16 v109, v16 offset:128
	v_add_f32_e32 v19, v162, v19
	v_fma_f32 v16, -v23, v25, 1.0
	v_fmac_f32_e32 v25, v16, v25
	v_div_scale_f32 v16, vcc, v17, v21, v17
	v_mul_f32_e32 v20, v16, v25
	v_fma_f32 v22, -v23, v20, v16
	v_fmac_f32_e32 v20, v22, v25
	v_mul_f32_e32 v22, 0x3d372713, v18
	v_mul_f32_e32 v22, v18, v22
	v_fma_f32 v22, v18, v22, v18
	v_mul_f32_e32 v22, 0x3f4c422a, v22
	v_mul_f32_e32 v22, 0xc038aa3b, v22
	v_exp_f32_e32 v22, v22
	v_fma_f32 v16, -v23, v20, v16
	v_div_fmas_f32 v16, v16, v25, v20
	v_div_fixup_f32 v16, v16, v21, v17
	v_add_f32_e32 v20, 1.0, v22
	v_div_scale_f32 v22, s[0:1], v20, v20, v18
	v_rcp_f32_e32 v23, v22
	s_nop 0
	v_cvt_pk_bf16_f32 v16, v16, s0
	ds_write_b16 v108, v16 offset:128
	v_add_f32_e32 v12, v162, v12
	v_fma_f32 v16, -v22, v23, 1.0
	v_fmac_f32_e32 v23, v16, v23
	v_div_scale_f32 v16, vcc, v18, v20, v18
	v_mul_f32_e32 v17, v16, v23
	v_fma_f32 v21, -v22, v17, v16
	v_fmac_f32_e32 v17, v21, v23
	v_mul_f32_e32 v21, 0x3d372713, v19
	v_mul_f32_e32 v21, v19, v21
	v_fma_f32 v21, v19, v21, v19
	v_mul_f32_e32 v21, 0x3f4c422a, v21
	v_mul_f32_e32 v21, 0xc038aa3b, v21
	v_exp_f32_e32 v21, v21
	v_fma_f32 v16, -v22, v17, v16
	v_div_fmas_f32 v16, v16, v23, v17
	v_div_fixup_f32 v16, v16, v20, v18
	v_add_f32_e32 v17, 1.0, v21
	v_div_scale_f32 v21, s[0:1], v17, v17, v19
	v_rcp_f32_e32 v22, v21
	s_nop 0
	v_cvt_pk_bf16_f32 v16, v16, s0
	ds_write_b16 v34, v16 offset:128
	v_add_f32_e32 v13, v162, v13
	v_fma_f32 v16, -v21, v22, 1.0
	v_fmac_f32_e32 v22, v16, v22
	v_div_scale_f32 v16, vcc, v19, v17, v19
	v_mul_f32_e32 v18, v16, v22
	v_fma_f32 v20, -v21, v18, v16
	v_fmac_f32_e32 v18, v20, v22
	v_mul_f32_e32 v20, 0x3d372713, v12
	v_mul_f32_e32 v20, v12, v20
	v_fma_f32 v20, v12, v20, v12
	v_mul_f32_e32 v20, 0x3f4c422a, v20
	v_mul_f32_e32 v20, 0xc038aa3b, v20
	v_exp_f32_e32 v20, v20
	v_fma_f32 v16, -v21, v18, v16
	v_div_fmas_f32 v16, v16, v22, v18
	v_div_fixup_f32 v16, v16, v17, v19
	v_add_f32_e32 v18, 1.0, v20
	v_div_scale_f32 v20, s[0:1], v18, v18, v12
	v_rcp_f32_e32 v21, v20
	s_nop 0
	v_cvt_pk_bf16_f32 v16, v16, s0
	ds_write_b16 v33, v16 offset:128
	v_add_f32_e32 v14, v162, v14
	v_fma_f32 v16, -v20, v21, 1.0
	v_fmac_f32_e32 v21, v16, v21
	v_div_scale_f32 v16, vcc, v12, v18, v12
	v_mul_f32_e32 v17, v16, v21
	v_fma_f32 v19, -v20, v17, v16
	v_fmac_f32_e32 v17, v19, v21
	v_mul_f32_e32 v19, 0x3d372713, v13
	v_mul_f32_e32 v19, v13, v19
	v_fma_f32 v19, v13, v19, v13
	v_mul_f32_e32 v19, 0x3f4c422a, v19
	v_mul_f32_e32 v19, 0xc038aa3b, v19
	v_exp_f32_e32 v19, v19
	v_fma_f32 v16, -v20, v17, v16
	v_div_fmas_f32 v16, v16, v21, v17
	v_div_fixup_f32 v12, v16, v18, v12
	v_add_f32_e32 v17, 1.0, v19
	v_div_scale_f32 v19, s[0:1], v17, v17, v13
	v_rcp_f32_e32 v20, v19
	s_nop 0
	v_cvt_pk_bf16_f32 v12, v12, s0
	ds_write_b16 v32, v12 offset:128
	v_add_f32_e32 v15, v162, v15
	v_fma_f32 v12, -v19, v20, 1.0
	v_fmac_f32_e32 v20, v12, v20
	v_div_scale_f32 v12, vcc, v13, v17, v13
	v_mul_f32_e32 v16, v12, v20
	v_fma_f32 v18, -v19, v16, v12
	v_fmac_f32_e32 v16, v18, v20
	v_mul_f32_e32 v18, 0x3d372713, v14
	v_mul_f32_e32 v18, v14, v18
	v_fma_f32 v18, v14, v18, v14
	v_mul_f32_e32 v18, 0x3f4c422a, v18
	v_mul_f32_e32 v18, 0xc038aa3b, v18
	v_exp_f32_e32 v18, v18
	v_fma_f32 v12, -v19, v16, v12
	v_div_fmas_f32 v12, v12, v20, v16
	v_div_fixup_f32 v12, v12, v17, v13
	v_add_f32_e32 v16, 1.0, v18
	v_div_scale_f32 v18, s[0:1], v16, v16, v14
	v_rcp_f32_e32 v19, v18
	s_nop 0
	v_cvt_pk_bf16_f32 v12, v12, s0
	ds_write_b16 v29, v12 offset:128
	s_waitcnt vmcnt(18)
	v_add_f32_e32 v8, v160, v8
	v_fma_f32 v12, -v18, v19, 1.0
	v_fmac_f32_e32 v19, v12, v19
	v_div_scale_f32 v12, vcc, v14, v16, v14
	v_mul_f32_e32 v13, v12, v19
	v_fma_f32 v17, -v18, v13, v12
	v_fmac_f32_e32 v13, v17, v19
	v_mul_f32_e32 v17, 0x3d372713, v15
	v_mul_f32_e32 v17, v15, v17
	v_fma_f32 v17, v15, v17, v15
	v_mul_f32_e32 v17, 0x3f4c422a, v17
	v_mul_f32_e32 v17, 0xc038aa3b, v17
	v_exp_f32_e32 v17, v17
	v_fma_f32 v12, -v18, v13, v12
	v_div_fmas_f32 v12, v12, v19, v13
	v_div_fixup_f32 v12, v12, v16, v14
	v_add_f32_e32 v13, 1.0, v17
	v_div_scale_f32 v17, s[0:1], v13, v13, v15
	v_rcp_f32_e32 v18, v17
	s_nop 0
	v_cvt_pk_bf16_f32 v12, v12, s0
	ds_write_b16 v28, v12 offset:128
	v_add_f32_e32 v9, v160, v9
	v_fma_f32 v12, -v17, v18, 1.0
	v_fmac_f32_e32 v18, v12, v18
	v_div_scale_f32 v12, vcc, v15, v13, v15
	v_mul_f32_e32 v14, v12, v18
	v_fma_f32 v16, -v17, v14, v12
	v_fmac_f32_e32 v14, v16, v18
	v_mul_f32_e32 v16, 0x3d372713, v8
	v_mul_f32_e32 v16, v8, v16
	v_fma_f32 v16, v8, v16, v8
	v_mul_f32_e32 v16, 0x3f4c422a, v16
	v_mul_f32_e32 v16, 0xc038aa3b, v16
	v_exp_f32_e32 v16, v16
	v_fma_f32 v12, -v17, v14, v12
	v_div_fmas_f32 v12, v12, v18, v14
	v_div_fixup_f32 v12, v12, v13, v15
	v_add_f32_e32 v14, 1.0, v16
	v_div_scale_f32 v16, s[0:1], v14, v14, v8
	v_rcp_f32_e32 v17, v16
	s_nop 0
	v_cvt_pk_bf16_f32 v12, v12, s0
	ds_write_b16 v24, v12 offset:128
	v_add_f32_e32 v10, v160, v10
	v_fma_f32 v12, -v16, v17, 1.0
	v_fmac_f32_e32 v17, v12, v17
	v_div_scale_f32 v12, vcc, v8, v14, v8
	v_mul_f32_e32 v13, v12, v17
	v_fma_f32 v15, -v16, v13, v12
	v_fmac_f32_e32 v13, v15, v17
	v_mul_f32_e32 v15, 0x3d372713, v9
	v_mul_f32_e32 v15, v9, v15
	v_fma_f32 v15, v9, v15, v9
	v_mul_f32_e32 v15, 0x3f4c422a, v15
	v_mul_f32_e32 v15, 0xc038aa3b, v15
	v_exp_f32_e32 v15, v15
	v_fma_f32 v12, -v16, v13, v12
	v_div_fmas_f32 v12, v12, v17, v13
	v_div_fixup_f32 v8, v12, v14, v8
	v_add_f32_e32 v13, 1.0, v15
	v_div_scale_f32 v15, s[0:1], v13, v13, v9
	v_rcp_f32_e32 v16, v15
	s_nop 0
	v_cvt_pk_bf16_f32 v8, v8, s0
	ds_write_b16 v109, v8 offset:160
	v_add_f32_e32 v11, v160, v11
	v_fma_f32 v8, -v15, v16, 1.0
	v_fmac_f32_e32 v16, v8, v16
	v_div_scale_f32 v8, vcc, v9, v13, v9
	v_mul_f32_e32 v12, v8, v16
	v_fma_f32 v14, -v15, v12, v8
	v_fmac_f32_e32 v12, v14, v16
	v_mul_f32_e32 v14, 0x3d372713, v10
	v_mul_f32_e32 v14, v10, v14
	v_fma_f32 v14, v10, v14, v10
	v_mul_f32_e32 v14, 0x3f4c422a, v14
	v_mul_f32_e32 v14, 0xc038aa3b, v14
	v_exp_f32_e32 v14, v14
	v_fma_f32 v8, -v15, v12, v8
	v_div_fmas_f32 v8, v8, v16, v12
	v_div_fixup_f32 v8, v8, v13, v9
	v_add_f32_e32 v12, 1.0, v14
	v_div_scale_f32 v14, s[0:1], v12, v12, v10
	v_rcp_f32_e32 v15, v14
	s_nop 0
	v_cvt_pk_bf16_f32 v8, v8, s0
	ds_write_b16 v108, v8 offset:160
	v_add_f32_e32 v4, v160, v4
	v_fma_f32 v8, -v14, v15, 1.0
	v_fmac_f32_e32 v15, v8, v15
	v_div_scale_f32 v8, vcc, v10, v12, v10
	v_mul_f32_e32 v9, v8, v15
	v_fma_f32 v13, -v14, v9, v8
	v_fmac_f32_e32 v9, v13, v15
	v_mul_f32_e32 v13, 0x3d372713, v11
	v_mul_f32_e32 v13, v11, v13
	v_fma_f32 v13, v11, v13, v11
	v_mul_f32_e32 v13, 0x3f4c422a, v13
	v_mul_f32_e32 v13, 0xc038aa3b, v13
	v_exp_f32_e32 v13, v13
	v_fma_f32 v8, -v14, v9, v8
	v_div_fmas_f32 v8, v8, v15, v9
	v_div_fixup_f32 v8, v8, v12, v10
	v_add_f32_e32 v9, 1.0, v13
	v_div_scale_f32 v13, s[0:1], v9, v9, v11
	v_rcp_f32_e32 v14, v13
	s_nop 0
	v_cvt_pk_bf16_f32 v8, v8, s0
	ds_write_b16 v34, v8 offset:160
	v_add_f32_e32 v5, v160, v5
	v_fma_f32 v8, -v13, v14, 1.0
	v_fmac_f32_e32 v14, v8, v14
	v_div_scale_f32 v8, vcc, v11, v9, v11
	v_mul_f32_e32 v10, v8, v14
	v_fma_f32 v12, -v13, v10, v8
	v_fmac_f32_e32 v10, v12, v14
	v_mul_f32_e32 v12, 0x3d372713, v4
	v_mul_f32_e32 v12, v4, v12
	v_fma_f32 v12, v4, v12, v4
	v_mul_f32_e32 v12, 0x3f4c422a, v12
	v_mul_f32_e32 v12, 0xc038aa3b, v12
	v_exp_f32_e32 v12, v12
	v_fma_f32 v8, -v13, v10, v8
	v_div_fmas_f32 v8, v8, v14, v10
	v_div_fixup_f32 v8, v8, v9, v11
	v_add_f32_e32 v10, 1.0, v12
	v_div_scale_f32 v12, s[0:1], v10, v10, v4
	v_rcp_f32_e32 v13, v12
	s_nop 0
	v_cvt_pk_bf16_f32 v8, v8, s0
	ds_write_b16 v33, v8 offset:160
	v_add_f32_e32 v6, v160, v6
	v_fma_f32 v8, -v12, v13, 1.0
	v_fmac_f32_e32 v13, v8, v13
	v_div_scale_f32 v8, vcc, v4, v10, v4
	v_mul_f32_e32 v9, v8, v13
	v_fma_f32 v11, -v12, v9, v8
	v_fmac_f32_e32 v9, v11, v13
	v_mul_f32_e32 v11, 0x3d372713, v5
	v_mul_f32_e32 v11, v5, v11
	v_fma_f32 v11, v5, v11, v5
	v_mul_f32_e32 v11, 0x3f4c422a, v11
	v_mul_f32_e32 v11, 0xc038aa3b, v11
	v_exp_f32_e32 v11, v11
	v_fma_f32 v8, -v12, v9, v8
	v_div_fmas_f32 v8, v8, v13, v9
	v_div_fixup_f32 v4, v8, v10, v4
	v_add_f32_e32 v9, 1.0, v11
	v_div_scale_f32 v11, s[0:1], v9, v9, v5
	v_rcp_f32_e32 v12, v11
	s_nop 0
	v_cvt_pk_bf16_f32 v4, v4, s0
	ds_write_b16 v32, v4 offset:160
	v_add_f32_e32 v7, v160, v7
	v_fma_f32 v4, -v11, v12, 1.0
	v_fmac_f32_e32 v12, v4, v12
	v_div_scale_f32 v4, vcc, v5, v9, v5
	v_mul_f32_e32 v8, v4, v12
	v_fma_f32 v10, -v11, v8, v4
	v_fmac_f32_e32 v8, v10, v12
	v_mul_f32_e32 v10, 0x3d372713, v6
	v_mul_f32_e32 v10, v6, v10
	v_fma_f32 v10, v6, v10, v6
	v_mul_f32_e32 v10, 0x3f4c422a, v10
	v_mul_f32_e32 v10, 0xc038aa3b, v10
	v_exp_f32_e32 v10, v10
	v_fma_f32 v4, -v11, v8, v4
	v_div_fmas_f32 v4, v4, v12, v8
	v_div_fixup_f32 v4, v4, v9, v5
	v_add_f32_e32 v8, 1.0, v10
	v_div_scale_f32 v10, s[0:1], v8, v8, v6
	v_rcp_f32_e32 v11, v10
	s_nop 0
	v_cvt_pk_bf16_f32 v4, v4, s0
	ds_write_b16 v29, v4 offset:160
	v_lshl_add_u64 v[26:27], s[22:23], 0, v[2:3]
	v_fma_f32 v4, -v10, v11, 1.0
	v_fmac_f32_e32 v11, v4, v11
	v_div_scale_f32 v4, vcc, v6, v8, v6
	v_mul_f32_e32 v5, v4, v11
	v_fma_f32 v9, -v10, v5, v4
	v_fmac_f32_e32 v5, v9, v11
	v_mul_f32_e32 v9, 0x3d372713, v7
	v_mul_f32_e32 v9, v7, v9
	v_fma_f32 v9, v7, v9, v7
	v_mul_f32_e32 v9, 0x3f4c422a, v9
	v_mul_f32_e32 v9, 0xc038aa3b, v9
	v_exp_f32_e32 v9, v9
	v_fma_f32 v4, -v10, v5, v4
	v_div_fmas_f32 v4, v4, v11, v5
	v_div_fixup_f32 v4, v4, v8, v6
	v_add_f32_e32 v5, 1.0, v9
	v_div_scale_f32 v9, s[0:1], v5, v5, v7
	v_rcp_f32_e32 v10, v9
	s_nop 0
	v_cvt_pk_bf16_f32 v4, v4, s0
	ds_write_b16 v28, v4 offset:160
	v_lshl_add_u64 v[28:29], s[22:23], 0, v[154:155]
	v_fma_f32 v4, -v9, v10, 1.0
	v_fmac_f32_e32 v10, v4, v10
	v_div_scale_f32 v4, vcc, v7, v5, v7
	v_mul_f32_e32 v6, v4, v10
	v_fma_f32 v8, -v9, v6, v4
	v_fmac_f32_e32 v6, v8, v10
	v_fma_f32 v4, -v9, v6, v4
	v_div_fmas_f32 v4, v4, v10, v6
	v_div_fixup_f32 v4, v4, v5, v7
	v_cvt_pk_bf16_f32 v4, v4, s0
	s_movk_i32 s0, 0x308
	v_mad_u32_u24 v2, v171, s0, v172
	ds_write_b16 v24, v4 offset:160
	v_lshl_add_u64 v[30:31], s[22:23], 0, v[156:157]
	v_lshlrev_b32_e32 v32, 1, v2
	s_movk_i32 s0, 0x1000
	v_mov_b32_e32 v2, v3
	v_mov_b32_e32 v4, v3
	v_mov_b32_e32 v5, v3
	v_mov_b32_e32 v6, v3
	v_mov_b32_e32 v7, v3
	v_mov_b32_e32 v8, v3
	v_mov_b32_e32 v9, v3
	v_mov_b32_e32 v10, v3
	v_mov_b32_e32 v11, v3
	v_mov_b32_e32 v12, v3
	v_mov_b32_e32 v13, v3
	v_mov_b32_e32 v14, v3
	v_mov_b32_e32 v15, v3
	v_mov_b32_e32 v16, v3
	v_mov_b32_e32 v17, v3
	v_mov_b32_e32 v18, v3
	v_mov_b32_e32 v19, v3
	v_mov_b32_e32 v20, v3
	v_mov_b32_e32 v21, v3
	v_mov_b32_e32 v22, v3
	v_mov_b32_e32 v23, v3
	v_mov_b32_e32 v24, v3
	v_mov_b32_e32 v25, v3
	s_waitcnt lgkmcnt(0)
	s_barrier
